# tail phase: second token's row loads issued together with the first token's (8 KB per wave in flight instead of 4)
# speedup vs baseline: 1.0021x; 1.0021x over previous
; DI void phase_tail(const Frame& F, int l) {
;     ...
;         for (int q = 0; q < 4; ++q) {
;             const int tkl = 4 * F.wave + q, t = 32 * ti + tkl;
;             f32x4 y[4], x[4], hv[4];
;             load_bf16_row((const bf16_t*)(F.ws + WS_Y) + (size_t)t * D, F.lane, y);
;             load_bf16_row((const bf16_t*)(F.ws + WS_XB) + (size_t)t * D, F.lane, x);
;             const float rstd = rms_rstd(y);
; #pragma unroll
;             for (int j = 0; j < 4; ++j) x[j] = x[j] + Bv[j] * (y[j] * rstd);
;             store_bf16_row((bf16_t*)(F.ws + WS_XB) + (size_t)t * D, F.lane, x);
.LBB0_960:
	v_lshl_add_u64 v[100:101], s[54:55], 0, v[62:63]
	v_add_co_u32_e32 v102, vcc, 0x94000000, v100
	s_brev_b32 s2, 23
	s_nop 0
	v_addc_co_u32_e32 v103, vcc, 0, v101, vcc
	v_add_co_u32_e32 v116, vcc, s2, v100
	global_load_dwordx4 v[124:127], v[102:103], off
	global_load_dwordx4 v[144:147], v[102:103], off offset:1024
	v_addc_co_u32_e32 v117, vcc, 0, v101, vcc
	global_load_dwordx4 v[110:113], v[116:117], off
	global_load_dwordx4 v[118:121], v[116:117], off offset:1024
	s_ashr_i32 s47, s46, 31
	s_lshl_b64 s[66:67], s[46:47], 10
	s_lshl_b64 s[68:69], s[46:47], 11
	v_lshl_add_u64 v[176:177], v[54:55], 0, s[68:69]
	v_lshl_add_u64 v[178:179], v[56:57], 0, s[68:69]
	global_load_dwordx4 v[160:163], v[176:177], off
	global_load_dwordx4 v[164:167], v[176:177], off offset:1024
	global_load_dwordx4 v[168:171], v[178:179], off
	global_load_dwordx4 v[172:175], v[178:179], off offset:1024
	v_lshl_add_u64 v[62:63], v[62:63], 0, s[0:1]
	s_waitcnt vmcnt(7)
	v_lshlrev_b32_e32 v128, 16, v125
	s_waitcnt vmcnt(6)
	v_lshlrev_b32_e32 v108, 16, v146
	v_and_b32_e32 v143, 0xffff0000, v146
	v_lshlrev_b32_e32 v114, 16, v147
	s_waitcnt vmcnt(5)
	v_lshlrev_b32_e32 v102, 16, v110
	v_and_b32_e32 v103, 0xffff0000, v110
	v_lshlrev_b32_e32 v110, 16, v124
	v_lshlrev_b32_e32 v100, 16, v111
	v_and_b32_e32 v101, 0xffff0000, v111
	v_and_b32_e32 v111, 0xffff0000, v124
	v_mul_f32_e32 v124, v110, v110
	v_and_b32_e32 v115, 0xffff0000, v147
	v_pk_fma_f32 v[146:147], v[110:111], v[110:111], v[124:125] op_sel_hi:[1,1,0]
	v_and_b32_e32 v129, 0xffff0000, v125
	v_mul_f32_e32 v124, v128, v128
	v_pk_fma_f32 v[148:149], v[128:129], v[128:129], v[124:125] op_sel_hi:[1,1,0]
	v_lshlrev_b32_e32 v125, 16, v127
	v_lshlrev_b32_e32 v124, 16, v126
	v_and_b32_e32 v127, 0xffff0000, v127
	v_and_b32_e32 v126, 0xffff0000, v126
	v_pk_mul_f32 v[130:131], v[126:127], v[126:127]
	v_mov_b32_e32 v109, v147
	v_pk_fma_f32 v[130:131], v[124:125], v[124:125], v[130:131]
	v_mov_b32_e32 v154, v108
	v_pk_add_f32 v[150:151], v[130:131], v[130:131] op_sel_hi:[0,1]
	v_lshlrev_b32_e32 v130, 16, v144
	v_and_b32_e32 v131, 0xffff0000, v144
	v_mul_f32_e32 v132, v130, v130
	v_pk_fma_f32 v[152:153], v[130:131], v[130:131], v[132:133] op_sel_hi:[1,1,0]
	v_lshlrev_b32_e32 v132, 16, v145
	v_and_b32_e32 v133, 0xffff0000, v145
	v_mul_f32_e32 v144, v132, v132
	v_mov_b32_e32 v155, v149
	v_pk_fma_f32 v[144:145], v[132:133], v[132:133], v[144:145] op_sel_hi:[1,1,0]
	v_pk_mul_f32 v[154:155], v[108:109], v[154:155]
	v_pk_add_f32 v[146:147], v[146:147], v[148:149]
	v_mul_f32_e32 v150, v143, v143
	v_mul_f32_e32 v152, v114, v114
	v_mul_f32_e32 v144, v115, v115
	v_mov_b32_e32 v155, v147
	v_pk_add_f32 v[146:147], v[154:155], v[150:151]
	v_pk_add_f32 v[144:145], v[152:153], v[144:145]
	v_lshlrev_b32_e32 v106, 16, v112
	v_pk_add_f32 v[144:145], v[146:147], v[144:145]
	v_and_b32_e32 v107, 0xffff0000, v112
	v_add_f32_e32 v109, v144, v145
	s_waitcnt vmcnt(4)
	v_lshlrev_b32_e32 v122, 16, v119
	v_and_b32_e32 v123, 0xffff0000, v119
	v_add_f32_dpp v109, v109, v109 quad_perm:[1,0,3,2] row_mask:0xf bank_mask:0xf bound_ctrl:1
	v_lshlrev_b32_e32 v104, 16, v113
	v_and_b32_e32 v105, 0xffff0000, v113
	v_add_f32_dpp v109, v109, v109 quad_perm:[2,3,0,1] row_mask:0xf bank_mask:0xf bound_ctrl:1
	v_lshlrev_b32_e32 v112, 16, v118
	v_and_b32_e32 v113, 0xffff0000, v118
	v_add_f32_dpp v109, v109, v109 row_half_mirror row_mask:0xf bank_mask:0xf bound_ctrl:1
	v_lshlrev_b32_e32 v118, 16, v120
	v_and_b32_e32 v119, 0xffff0000, v120
	v_add_f32_dpp v109, v109, v109 row_mirror row_mask:0xf bank_mask:0xf bound_ctrl:1
	v_lshlrev_b32_e32 v120, 16, v121
	v_readlane_b32 s2, v109, 16
	v_readlane_b32 s5, v109, 48
	v_readlane_b32 s6, v109, 0
	v_readlane_b32 s7, v109, 32
	v_mov_b32_e32 v144, s2
	v_mov_b32_e32 v145, s5
	v_pk_add_f32 v[144:145], s[6:7], v[144:145]
	v_and_b32_e32 v121, 0xffff0000, v121
	v_add_f32_e32 v109, v144, v145
	v_mov_b32_e32 v144, 0x358637bd
	s_nop 0
	v_fmac_f32_e32 v144, 0x3a800000, v109
	v_rsq_f32_e32 v144, v144
	v_mov_b32_e32 v109, v143
	v_add_u32_e32 v143, s4, v139
	s_addk_i32 s4, 0x1020
	v_pk_mul_f32 v[110:111], v[144:145], v[110:111] op_sel_hi:[0,1]
	v_pk_fma_f32 v[102:103], v[70:71], v[110:111], v[102:103]
	v_mov_b32_e32 v110, v124
	v_mov_b32_e32 v111, v126
	v_pk_mul_f32 v[110:111], v[144:145], v[110:111] op_sel_hi:[0,1]
	v_pk_fma_f32 v[110:111], v[74:75], v[110:111], v[106:107]
	v_pk_mul_f32 v[106:107], v[144:145], v[132:133] op_sel_hi:[0,1]
	v_pk_fma_f32 v[106:107], v[76:77], v[106:107], v[122:123]
	v_pk_mul_f32 v[122:123], v[108:109], v[144:145] op_sel_hi:[1,0]
	v_pk_mul_f32 v[108:109], v[114:115], v[144:145] op_sel_hi:[1,0]
	v_pk_fma_f32 v[114:115], v[82:83], v[122:123], v[118:119]
	v_bfe_u32 v118, v102, 16, 1
	v_pk_mul_f32 v[128:129], v[144:145], v[128:129] op_sel_hi:[0,1]
	v_add3_u32 v118, v102, v118, s15
	v_bfe_u32 v119, v103, 16, 1
	v_pk_fma_f32 v[100:101], v[68:69], v[128:129], v[100:101]
	v_lshrrev_b32_e32 v118, 16, v118
	v_add3_u32 v119, v103, v119, s15
	v_and_or_b32 v118, v119, s16, v118
	v_bfe_u32 v119, v100, 16, 1
	v_pk_fma_f32 v[108:109], v[80:81], v[108:109], v[120:121]
	v_add3_u32 v119, v100, v119, s15
	v_bfe_u32 v120, v101, 16, 1
	v_lshrrev_b32_e32 v119, 16, v119
	v_add3_u32 v120, v101, v120, s15
	v_mov_b32_e32 v126, v125
	v_and_or_b32 v119, v120, s16, v119
	v_bfe_u32 v120, v110, 16, 1
	v_pk_mul_f32 v[124:125], v[144:145], v[126:127] op_sel_hi:[0,1]
	v_add3_u32 v120, v110, v120, s15
	v_bfe_u32 v121, v111, 16, 1
	v_pk_fma_f32 v[104:105], v[72:73], v[124:125], v[104:105]
	v_lshrrev_b32_e32 v120, 16, v120
	v_add3_u32 v121, v111, v121, s15
	v_and_or_b32 v120, v121, s16, v120
	v_bfe_u32 v121, v104, 16, 1
	v_add3_u32 v121, v104, v121, s15
; #define LAS __attribute__((address_space(3)))
; DI unsigned pk2(float lo, float hi) { return f2bf(lo) | (f2bf(hi) << 16); }
; DI unsigned pk_fp8x4(float a, float b, float c, float d) { int p = 0; p = __builtin_amdgcn_cvt_pk_fp8_f32(a, b, p, false); p = __builtin_amdgcn_cvt_pk_fp8_f32(c, d, p, true); return (unsigned)p; }
; DI void phase_tail(const Frame& F, int l) {
;     ...
;             for (int j = 0; j < 4; ++j) x[j] = x[j] + Bv[j] * (y[j] * rstd);
;             store_bf16_row((bf16_t*)(F.ws + WS_XB) + (size_t)t * D, F.lane, x);
;             { const float rs2 = rms_rstd(x);
; #pragma unroll
;               for (int j = 0; j < 4; ++j) hv[j] = x[j] * rs2 * Av[j] + Sv[j];
; #pragma unroll
;               for (int g = 0; g < 2; ++g) { u32x2 w; w.x = pk_fp8x4(hv[2 * g].x, hv[2 * g].y, hv[2 * g].z, hv[2 * g].w); w.y = pk_fp8x4(hv[2 * g + 1].x, hv[2 * g + 1].y, hv[2 * g + 1].z, hv[2 * g + 1].w);
;                   *(u32x2*)((unsigned char*)(F.ws + WS_H8) + (size_t)t * D + 8 * F.lane + 512 * g) = w; } }
; #pragma unroll
;             for (int g = 0; g < 2; ++g) { u32x4 w; w.x = pk2(hv[2 * g].x, hv[2 * g].y); w.y = pk2(hv[2 * g].z, hv[2 * g].w); w.z = pk2(hv[2 * g + 1].x, hv[2 * g + 1].y); w.w = pk2(hv[2 * g + 1].z, hv[2 * g + 1].w);
;                 *(LAS u32x4*)(Ht + tkl * HT_STRIDE + 8 * F.lane + 512 * g) = w; }
	v_bfe_u32 v122, v105, 16, 1
	v_pk_mul_f32 v[124:125], v[144:145], v[130:131] op_sel_hi:[0,1]
	v_lshrrev_b32_e32 v121, 16, v121
	v_add3_u32 v122, v105, v122, s15
	v_pk_fma_f32 v[112:113], v[78:79], v[124:125], v[112:113]
	v_and_or_b32 v121, v122, s16, v121
	global_store_dwordx4 v[116:117], v[118:121], off
	v_bfe_u32 v122, v109, 16, 1
	v_add3_u32 v122, v109, v122, s15
	v_bfe_u32 v118, v112, 16, 1
	v_add3_u32 v118, v112, v118, s15
	v_bfe_u32 v119, v113, 16, 1
	v_lshrrev_b32_e32 v118, 16, v118
	v_add3_u32 v119, v113, v119, s15
	v_and_or_b32 v118, v119, s16, v118
	v_bfe_u32 v119, v106, 16, 1
	v_add3_u32 v119, v106, v119, s15
	v_bfe_u32 v120, v107, 16, 1
	v_lshrrev_b32_e32 v119, 16, v119
	v_add3_u32 v120, v107, v120, s15
	v_and_or_b32 v119, v120, s16, v119
	v_bfe_u32 v120, v114, 16, 1
	v_add3_u32 v120, v114, v120, s15
	v_bfe_u32 v121, v115, 16, 1
	v_lshrrev_b32_e32 v120, 16, v120
	v_add3_u32 v121, v115, v121, s15
	v_and_or_b32 v120, v121, s16, v120
	v_bfe_u32 v121, v108, 16, 1
	v_add3_u32 v121, v108, v121, s15
	v_lshrrev_b32_e32 v121, 16, v121
	v_and_or_b32 v121, v122, s16, v121
	global_store_dwordx4 v[116:117], v[118:121], off offset:1024
	v_pk_mul_f32 v[116:117], v[100:101], v[100:101]
	s_nop 0
	v_pk_mul_f32 v[118:119], v[102:103], v[102:103]
	s_nop 0
	v_pk_mov_b32 v[120:121], v[118:119], v[116:117] op_sel:[1,0]
	v_mov_b32_e32 v119, v117
	v_pk_add_f32 v[116:117], v[120:121], v[118:119]
	v_pk_mul_f32 v[118:119], v[104:105], v[104:105]
	v_pk_add_f32 v[116:117], v[116:117], v[116:117] op_sel_hi:[0,1]
	v_pk_mul_f32 v[120:121], v[110:111], v[110:111]
	v_mul_f32_e32 v116, v112, v112
	v_pk_mov_b32 v[122:123], v[120:121], v[118:119] op_sel:[1,0]
	v_mov_b32_e32 v121, v119
	v_pk_add_f32 v[118:119], v[122:123], v[120:121]
	v_pk_fma_f32 v[120:121], v[112:113], v[112:113], v[116:117] op_sel_hi:[1,1,0]
	v_mul_f32_e32 v116, v106, v106
	v_pk_add_f32 v[118:119], v[118:119], v[118:119] op_sel_hi:[0,1]
	v_pk_fma_f32 v[122:123], v[106:107], v[106:107], v[116:117] op_sel_hi:[1,1,0]
	v_mul_f32_e32 v120, v114, v114
	v_mul_f32_e32 v122, v115, v115
	v_mul_f32_e32 v116, v108, v108
	v_mul_f32_e32 v118, v109, v109
	v_pk_add_f32 v[120:121], v[120:121], v[122:123]
	v_pk_add_f32 v[116:117], v[116:117], v[118:119]
	s_nop 0
	v_pk_add_f32 v[116:117], v[120:121], v[116:117]
	s_nop 0
	v_add_f32_e32 v116, v116, v117
	s_nop 1
	v_add_f32_dpp v116, v116, v116 quad_perm:[1,0,3,2] row_mask:0xf bank_mask:0xf bound_ctrl:1
	s_nop 1
	v_add_f32_dpp v116, v116, v116 quad_perm:[2,3,0,1] row_mask:0xf bank_mask:0xf bound_ctrl:1
	s_nop 1
	v_add_f32_dpp v116, v116, v116 row_half_mirror row_mask:0xf bank_mask:0xf bound_ctrl:1
	s_nop 1
	v_add_f32_dpp v116, v116, v116 row_mirror row_mask:0xf bank_mask:0xf bound_ctrl:1
	s_nop 0
	v_readlane_b32 s2, v116, 16
	v_readlane_b32 s5, v116, 48
	v_readlane_b32 s6, v116, 0
	v_readlane_b32 s7, v116, 32
	v_mov_b32_e32 v116, s2
	v_mov_b32_e32 v117, s5
	v_pk_add_f32 v[116:117], s[6:7], v[116:117]
	s_lshl_b64 s[6:7], s[46:47], 11
	v_add_f32_e32 v116, v116, v117
	v_mov_b32_e32 v117, 0x358637bd
	s_add_i32 s46, s46, 2
	v_fmac_f32_e32 v117, 0x3a800000, v116
	v_rsq_f32_e32 v116, v117
	s_cmpk_eq_i32 s4, 0x2040
	v_pk_mul_f32 v[100:101], v[100:101], v[116:117] op_sel_hi:[1,0]
	v_pk_mul_f32 v[102:103], v[102:103], v[116:117] op_sel_hi:[1,0]
	v_pk_fma_f32 v[118:119], v[84:85], v[100:101], v[6:7]
	v_pk_mul_f32 v[100:101], v[110:111], v[116:117] op_sel_hi:[1,0]
	v_pk_fma_f32 v[120:121], v[86:87], v[102:103], v[4:5]
	v_pk_mul_f32 v[102:103], v[104:105], v[116:117] op_sel_hi:[1,0]
	v_pk_fma_f32 v[110:111], v[90:91], v[100:101], v[0:1]
	v_pk_mul_f32 v[100:101], v[112:113], v[116:117] op_sel_hi:[1,0]
	v_pk_fma_f32 v[122:123], v[88:89], v[102:103], v[2:3]
	v_pk_mul_f32 v[102:103], v[106:107], v[116:117] op_sel_hi:[1,0]
	v_pk_fma_f32 v[106:107], v[94:95], v[100:101], v[12:13]
	v_pk_mul_f32 v[100:101], v[108:109], v[116:117] op_sel_hi:[1,0]
	v_mov_b32_e32 v108, v193
	v_mov_b32_e32 v109, v193
	v_cvt_pk_fp8_f32 v108, v120, v121
	v_cvt_pk_fp8_f32 v109, v110, v111
	v_lshl_add_u64 v[112:113], s[54:55], 0, v[64:65]
	v_add_co_u32_e32 v112, vcc, s18, v112
	v_cvt_pk_fp8_f32 v108, v118, v119 op_sel:[0,0,1]
	v_cvt_pk_fp8_f32 v109, v122, v123 op_sel:[0,0,1]
	v_pk_fma_f32 v[104:105], v[92:93], v[102:103], v[14:15]
	v_pk_mul_f32 v[102:103], v[114:115], v[116:117] op_sel_hi:[1,0]
	v_addc_co_u32_e32 v113, vcc, 0, v113, vcc
	v_pk_fma_f32 v[102:103], v[98:99], v[102:103], v[8:9]
	global_store_dwordx2 v[112:113], v[108:109], off
	v_mov_b32_e32 v108, v193
	v_mov_b32_e32 v109, v193
	v_cvt_pk_fp8_f32 v108, v106, v107
	v_cvt_pk_fp8_f32 v109, v102, v103
	v_pk_fma_f32 v[100:101], v[96:97], v[100:101], v[10:11]
	v_lshl_add_u64 v[116:117], v[56:57], 0, s[6:7]
	v_cvt_pk_fp8_f32 v108, v104, v105 op_sel:[0,0,1]
	v_cvt_pk_fp8_f32 v109, v100, v101 op_sel:[0,0,1]
	v_lshl_add_u64 v[64:65], v[64:65], 0, s[34:35]
	global_store_dwordx2 v[112:113], v[108:109], off offset:512
	v_bfe_u32 v108, v120, 16, 1
	v_add3_u32 v108, v120, v108, s15
	v_bfe_u32 v109, v121, 16, 1
	v_lshrrev_b32_e32 v108, 16, v108
	v_add3_u32 v109, v121, v109, s15
	v_and_or_b32 v108, v109, s16, v108
	v_bfe_u32 v109, v118, 16, 1
	v_add3_u32 v109, v118, v109, s15
	v_bfe_u32 v112, v119, 16, 1
	v_lshrrev_b32_e32 v109, 16, v109
	v_add3_u32 v112, v119, v112, s15
	v_and_or_b32 v109, v112, s16, v109
	v_bfe_u32 v112, v110, 16, 1
	v_add3_u32 v110, v110, v112, s15
	v_bfe_u32 v112, v111, 16, 1
	v_lshrrev_b32_e32 v110, 16, v110
	v_add3_u32 v111, v111, v112, s15
	v_and_or_b32 v110, v111, s16, v110
	v_bfe_u32 v111, v122, 16, 1
	v_add3_u32 v111, v122, v111, s15
	v_bfe_u32 v112, v123, 16, 1
	v_lshrrev_b32_e32 v111, 16, v111
	v_add3_u32 v112, v123, v112, s15
	v_and_or_b32 v111, v112, s16, v111
	ds_write_b128 v143, v[108:111]
	v_bfe_u32 v108, v106, 16, 1
	v_add3_u32 v106, v106, v108, s15
	v_bfe_u32 v108, v107, 16, 1
	v_lshrrev_b32_e32 v106, 16, v106
	v_add3_u32 v107, v107, v108, s15
	v_and_or_b32 v106, v107, s16, v106
	v_bfe_u32 v107, v104, 16, 1
	v_add3_u32 v104, v104, v107, s15
	v_bfe_u32 v107, v105, 16, 1
	v_lshrrev_b32_e32 v104, 16, v104
	v_add3_u32 v105, v105, v107, s15
	v_and_or_b32 v107, v105, s16, v104
	v_bfe_u32 v104, v102, 16, 1
	v_add3_u32 v102, v102, v104, s15
	v_bfe_u32 v104, v103, 16, 1
	v_lshrrev_b32_e32 v102, 16, v102
	v_add3_u32 v103, v103, v104, s15
	v_and_or_b32 v108, v103, s16, v102
	v_bfe_u32 v102, v100, 16, 1
	v_add3_u32 v100, v100, v102, s15
	v_bfe_u32 v102, v101, 16, 1
	v_lshrrev_b32_e32 v100, 16, v100
	v_add3_u32 v101, v101, v102, s15
	v_and_or_b32 v109, v101, s16, v100
	ds_write_b128 v143, v[106:109] offset:1024
	v_lshl_add_u64 v[100:101], v[54:55], 0, s[6:7]
	s_waitcnt vmcnt(4)
; DI void phase_tail(const Frame& F, int l) {
;     ...
;             load_bf16_row((const bf16_t*)(F.ws + WS_Y) + (size_t)t * D, F.lane, y);
;             load_bf16_row((const bf16_t*)(F.ws + WS_XB) + (size_t)t * D, F.lane, x);
;             const float rstd = rms_rstd(y);
; #pragma unroll
;             for (int j = 0; j < 4; ++j) x[j] = x[j] + Bv[j] * (y[j] * rstd);
;             store_bf16_row((bf16_t*)(F.ws + WS_XB) + (size_t)t * D, F.lane, x);
	v_mov_b32_e32 v124, v160
	v_mov_b32_e32 v125, v161
	v_mov_b32_e32 v126, v162
	v_mov_b32_e32 v127, v163
	v_mov_b32_e32 v144, v164
	v_mov_b32_e32 v145, v165
	v_mov_b32_e32 v146, v166
	v_mov_b32_e32 v147, v167
	v_mov_b32_e32 v110, v168
	v_mov_b32_e32 v111, v169
	v_mov_b32_e32 v112, v170
	v_mov_b32_e32 v113, v171
	v_mov_b32_e32 v118, v172
	v_mov_b32_e32 v119, v173
	v_mov_b32_e32 v120, v174
	v_mov_b32_e32 v121, v175
	s_waitcnt vmcnt(3)
	v_lshlrev_b32_e32 v128, 16, v125
	s_waitcnt vmcnt(2)
	v_lshlrev_b32_e32 v108, 16, v146
	s_waitcnt vmcnt(1)
	v_lshlrev_b32_e32 v102, 16, v110
	v_and_b32_e32 v103, 0xffff0000, v110
	v_lshlrev_b32_e32 v110, 16, v124
	v_lshlrev_b32_e32 v100, 16, v111
	v_and_b32_e32 v101, 0xffff0000, v111
	v_and_b32_e32 v111, 0xffff0000, v124
	v_mul_f32_e32 v124, v110, v110
	v_and_b32_e32 v156, 0xffff0000, v146
	v_lshlrev_b32_e32 v114, 16, v147
	v_and_b32_e32 v115, 0xffff0000, v147
	v_pk_fma_f32 v[146:147], v[110:111], v[110:111], v[124:125] op_sel_hi:[1,1,0]
	v_and_b32_e32 v129, 0xffff0000, v125
	v_mul_f32_e32 v124, v128, v128
	v_pk_fma_f32 v[148:149], v[128:129], v[128:129], v[124:125] op_sel_hi:[1,1,0]
	v_lshlrev_b32_e32 v125, 16, v127
	v_lshlrev_b32_e32 v124, 16, v126
	v_and_b32_e32 v127, 0xffff0000, v127
	v_and_b32_e32 v126, 0xffff0000, v126
	v_pk_mul_f32 v[130:131], v[126:127], v[126:127]
	v_mov_b32_e32 v109, v147
	v_pk_fma_f32 v[130:131], v[124:125], v[124:125], v[130:131]
	v_mov_b32_e32 v154, v108
	v_pk_add_f32 v[150:151], v[130:131], v[130:131] op_sel_hi:[0,1]
	v_lshlrev_b32_e32 v130, 16, v144
	v_and_b32_e32 v131, 0xffff0000, v144
	v_mul_f32_e32 v132, v130, v130
	v_pk_fma_f32 v[152:153], v[130:131], v[130:131], v[132:133] op_sel_hi:[1,1,0]
	v_lshlrev_b32_e32 v132, 16, v145
	v_and_b32_e32 v133, 0xffff0000, v145
	v_mul_f32_e32 v144, v132, v132
	v_mov_b32_e32 v155, v149
	v_pk_fma_f32 v[144:145], v[132:133], v[132:133], v[144:145] op_sel_hi:[1,1,0]
	v_pk_mul_f32 v[154:155], v[108:109], v[154:155]
	v_pk_add_f32 v[146:147], v[146:147], v[148:149]
	v_mul_f32_e32 v150, v156, v156
	v_mul_f32_e32 v152, v114, v114
	v_mul_f32_e32 v144, v115, v115
	v_mov_b32_e32 v155, v147
	v_pk_add_f32 v[146:147], v[154:155], v[150:151]
	v_pk_add_f32 v[144:145], v[152:153], v[144:145]
	v_lshlrev_b32_e32 v106, 16, v112
	v_pk_add_f32 v[144:145], v[146:147], v[144:145]
	v_and_b32_e32 v107, 0xffff0000, v112
	v_add_f32_e32 v109, v144, v145
	s_waitcnt vmcnt(0)
	v_lshlrev_b32_e32 v122, 16, v119
	v_and_b32_e32 v123, 0xffff0000, v119
	v_add_f32_dpp v109, v109, v109 quad_perm:[1,0,3,2] row_mask:0xf bank_mask:0xf bound_ctrl:1
	v_lshlrev_b32_e32 v104, 16, v113
	v_and_b32_e32 v105, 0xffff0000, v113
	v_add_f32_dpp v109, v109, v109 quad_perm:[2,3,0,1] row_mask:0xf bank_mask:0xf bound_ctrl:1
	v_lshlrev_b32_e32 v112, 16, v118
	v_and_b32_e32 v113, 0xffff0000, v118
	v_add_f32_dpp v109, v109, v109 row_half_mirror row_mask:0xf bank_mask:0xf bound_ctrl:1
	v_lshlrev_b32_e32 v118, 16, v120
	v_and_b32_e32 v119, 0xffff0000, v120
	v_add_f32_dpp v109, v109, v109 row_mirror row_mask:0xf bank_mask:0xf bound_ctrl:1
	v_lshlrev_b32_e32 v120, 16, v121
	v_readlane_b32 s2, v109, 16
	v_readlane_b32 s5, v109, 48
	v_readlane_b32 s6, v109, 0
	v_readlane_b32 s7, v109, 32
	v_mov_b32_e32 v144, s2
	v_mov_b32_e32 v145, s5
	v_pk_add_f32 v[144:145], s[6:7], v[144:145]
	v_and_b32_e32 v121, 0xffff0000, v121
	v_add_f32_e32 v109, v144, v145
	v_mov_b32_e32 v144, 0x358637bd
	s_nop 0
	v_fmac_f32_e32 v144, 0x3a800000, v109
	v_rsq_f32_e32 v144, v144
	v_mov_b32_e32 v109, v156
	v_pk_mul_f32 v[110:111], v[144:145], v[110:111] op_sel_hi:[0,1]
	v_pk_fma_f32 v[102:103], v[70:71], v[110:111], v[102:103]
	v_mov_b32_e32 v110, v124
	v_mov_b32_e32 v111, v126
	v_pk_mul_f32 v[110:111], v[144:145], v[110:111] op_sel_hi:[0,1]
	v_pk_fma_f32 v[110:111], v[74:75], v[110:111], v[106:107]
	v_pk_mul_f32 v[106:107], v[144:145], v[132:133] op_sel_hi:[0,1]
	v_pk_fma_f32 v[106:107], v[76:77], v[106:107], v[122:123]
	v_pk_mul_f32 v[122:123], v[108:109], v[144:145] op_sel_hi:[1,0]
	v_pk_mul_f32 v[108:109], v[114:115], v[144:145] op_sel_hi:[1,0]
	v_pk_fma_f32 v[114:115], v[82:83], v[122:123], v[118:119]
	v_bfe_u32 v118, v102, 16, 1
	v_pk_mul_f32 v[128:129], v[144:145], v[128:129] op_sel_hi:[0,1]
	v_add3_u32 v118, v102, v118, s15
	v_bfe_u32 v119, v103, 16, 1
	v_pk_fma_f32 v[100:101], v[68:69], v[128:129], v[100:101]
	v_lshrrev_b32_e32 v118, 16, v118
	v_add3_u32 v119, v103, v119, s15
	v_and_or_b32 v118, v119, s16, v118
	v_bfe_u32 v119, v100, 16, 1
	v_pk_fma_f32 v[108:109], v[80:81], v[108:109], v[120:121]
	v_add3_u32 v119, v100, v119, s15
	v_bfe_u32 v120, v101, 16, 1
	v_lshrrev_b32_e32 v119, 16, v119
	v_add3_u32 v120, v101, v120, s15
	v_mov_b32_e32 v126, v125
	v_and_or_b32 v119, v120, s16, v119
	v_bfe_u32 v120, v110, 16, 1
	v_pk_mul_f32 v[124:125], v[144:145], v[126:127] op_sel_hi:[0,1]
	v_add3_u32 v120, v110, v120, s15
	v_bfe_u32 v121, v111, 16, 1
	v_pk_fma_f32 v[104:105], v[72:73], v[124:125], v[104:105]
	v_lshrrev_b32_e32 v120, 16, v120
	v_add3_u32 v121, v111, v121, s15
	v_and_or_b32 v120, v121, s16, v120
	v_bfe_u32 v121, v104, 16, 1
	v_add3_u32 v121, v104, v121, s15
	v_bfe_u32 v122, v105, 16, 1
	v_pk_mul_f32 v[124:125], v[144:145], v[130:131] op_sel_hi:[0,1]
	v_lshrrev_b32_e32 v121, 16, v121
	v_add3_u32 v122, v105, v122, s15
	v_pk_fma_f32 v[112:113], v[78:79], v[124:125], v[112:113]
	v_and_or_b32 v121, v122, s16, v121
	global_store_dwordx4 v[116:117], v[118:121], off
	v_bfe_u32 v122, v109, 16, 1
	v_add3_u32 v122, v109, v122, s15
	v_bfe_u32 v118, v112, 16, 1
	v_add3_u32 v118, v112, v118, s15
	v_bfe_u32 v119, v113, 16, 1
	v_lshrrev_b32_e32 v118, 16, v118
	v_add3_u32 v119, v113, v119, s15
	v_and_or_b32 v118, v119, s16, v118
; #define LAS __attribute__((address_space(3)))
; DI unsigned pk2(float lo, float hi) { return f2bf(lo) | (f2bf(hi) << 16); }
; DI unsigned pk_fp8x4(float a, float b, float c, float d) { int p = 0; p = __builtin_amdgcn_cvt_pk_fp8_f32(a, b, p, false); p = __builtin_amdgcn_cvt_pk_fp8_f32(c, d, p, true); return (unsigned)p; }
; DI void phase_tail(const Frame& F, int l) {
;     ...
;             store_bf16_row((bf16_t*)(F.ws + WS_XB) + (size_t)t * D, F.lane, x);
;             { const float rs2 = rms_rstd(x);
; #pragma unroll
;               for (int j = 0; j < 4; ++j) hv[j] = x[j] * rs2 * Av[j] + Sv[j];
; #pragma unroll
;               for (int g = 0; g < 2; ++g) { u32x2 w; w.x = pk_fp8x4(hv[2 * g].x, hv[2 * g].y, hv[2 * g].z, hv[2 * g].w); w.y = pk_fp8x4(hv[2 * g + 1].x, hv[2 * g + 1].y, hv[2 * g + 1].z, hv[2 * g + 1].w);
;                   *(u32x2*)((unsigned char*)(F.ws + WS_H8) + (size_t)t * D + 8 * F.lane + 512 * g) = w; } }
; #pragma unroll
;             for (int g = 0; g < 2; ++g) { u32x4 w; w.x = pk2(hv[2 * g].x, hv[2 * g].y); w.y = pk2(hv[2 * g].z, hv[2 * g].w); w.z = pk2(hv[2 * g + 1].x, hv[2 * g + 1].y); w.w = pk2(hv[2 * g + 1].z, hv[2 * g + 1].w);
;                 *(LAS u32x4*)(Ht + tkl * HT_STRIDE + 8 * F.lane + 512 * g) = w; }
;         }
	v_bfe_u32 v119, v106, 16, 1
	v_add3_u32 v119, v106, v119, s15
	v_bfe_u32 v120, v107, 16, 1
	v_lshrrev_b32_e32 v119, 16, v119
	v_add3_u32 v120, v107, v120, s15
	v_and_or_b32 v119, v120, s16, v119
	v_bfe_u32 v120, v114, 16, 1
	v_add3_u32 v120, v114, v120, s15
	v_bfe_u32 v121, v115, 16, 1
	v_lshrrev_b32_e32 v120, 16, v120
	v_add3_u32 v121, v115, v121, s15
	v_and_or_b32 v120, v121, s16, v120
	v_bfe_u32 v121, v108, 16, 1
	v_add3_u32 v121, v108, v121, s15
	v_lshrrev_b32_e32 v121, 16, v121
	v_and_or_b32 v121, v122, s16, v121
	global_store_dwordx4 v[116:117], v[118:121], off offset:1024
	v_pk_mul_f32 v[116:117], v[100:101], v[100:101]
	s_nop 0
	v_pk_mul_f32 v[118:119], v[102:103], v[102:103]
	s_nop 0
	v_pk_mov_b32 v[120:121], v[118:119], v[116:117] op_sel:[1,0]
	v_mov_b32_e32 v119, v117
	v_pk_add_f32 v[116:117], v[120:121], v[118:119]
	v_pk_mul_f32 v[118:119], v[104:105], v[104:105]
	v_pk_add_f32 v[116:117], v[116:117], v[116:117] op_sel_hi:[0,1]
	v_pk_mul_f32 v[120:121], v[110:111], v[110:111]
	v_mul_f32_e32 v116, v112, v112
	v_pk_mov_b32 v[122:123], v[120:121], v[118:119] op_sel:[1,0]
	v_mov_b32_e32 v121, v119
	v_pk_add_f32 v[118:119], v[122:123], v[120:121]
	v_pk_fma_f32 v[120:121], v[112:113], v[112:113], v[116:117] op_sel_hi:[1,1,0]
	v_mul_f32_e32 v116, v106, v106
	v_pk_add_f32 v[118:119], v[118:119], v[118:119] op_sel_hi:[0,1]
	v_pk_fma_f32 v[122:123], v[106:107], v[106:107], v[116:117] op_sel_hi:[1,1,0]
	v_mul_f32_e32 v120, v114, v114
	v_mul_f32_e32 v122, v115, v115
	v_mul_f32_e32 v116, v108, v108
	v_mul_f32_e32 v118, v109, v109
	v_pk_add_f32 v[120:121], v[120:121], v[122:123]
	v_pk_add_f32 v[116:117], v[116:117], v[118:119]
	s_nop 0
	v_pk_add_f32 v[116:117], v[120:121], v[116:117]
	s_nop 0
	v_add_f32_e32 v116, v116, v117
	s_nop 1
	v_add_f32_dpp v116, v116, v116 quad_perm:[1,0,3,2] row_mask:0xf bank_mask:0xf bound_ctrl:1
	s_nop 1
	v_add_f32_dpp v116, v116, v116 quad_perm:[2,3,0,1] row_mask:0xf bank_mask:0xf bound_ctrl:1
	s_nop 1
	v_add_f32_dpp v116, v116, v116 row_half_mirror row_mask:0xf bank_mask:0xf bound_ctrl:1
	s_nop 1
	v_add_f32_dpp v116, v116, v116 row_mirror row_mask:0xf bank_mask:0xf bound_ctrl:1
	s_nop 0
	v_readlane_b32 s2, v116, 16
	v_readlane_b32 s5, v116, 48
	v_readlane_b32 s6, v116, 0
	v_readlane_b32 s7, v116, 32
	v_mov_b32_e32 v116, s2
	v_mov_b32_e32 v117, s5
	v_pk_add_f32 v[116:117], s[6:7], v[116:117]
	s_nop 0
	v_add_f32_e32 v116, v116, v117
	v_mov_b32_e32 v117, 0x358637bd
	s_nop 0
	v_fmac_f32_e32 v117, 0x3a800000, v116
	v_rsq_f32_e32 v116, v117
	s_nop 0
	v_pk_mul_f32 v[102:103], v[102:103], v[116:117] op_sel_hi:[1,0]
	v_pk_mul_f32 v[100:101], v[100:101], v[116:117] op_sel_hi:[1,0]
	v_pk_mul_f32 v[104:105], v[104:105], v[116:117] op_sel_hi:[1,0]
	v_pk_fma_f32 v[118:119], v[84:85], v[100:101], v[6:7]
	v_pk_fma_f32 v[100:101], v[86:87], v[102:103], v[4:5]
	v_pk_mul_f32 v[102:103], v[110:111], v[116:117] op_sel_hi:[1,0]
	v_pk_mul_f32 v[110:111], v[112:113], v[116:117] op_sel_hi:[1,0]
	v_pk_fma_f32 v[102:103], v[90:91], v[102:103], v[0:1]
	v_pk_mul_f32 v[112:113], v[114:115], v[116:117] op_sel_hi:[1,0]
	v_mov_b32_e32 v114, v193
	v_mov_b32_e32 v115, v193
	v_cvt_pk_fp8_f32 v114, v100, v101
	v_cvt_pk_fp8_f32 v115, v102, v103
	v_pk_fma_f32 v[104:105], v[88:89], v[104:105], v[2:3]
	v_pk_mul_f32 v[106:107], v[106:107], v[116:117] op_sel_hi:[1,0]
	v_cvt_pk_fp8_f32 v114, v118, v119 op_sel:[0,0,1]
	v_cvt_pk_fp8_f32 v115, v104, v105 op_sel:[0,0,1]
	v_pk_mul_f32 v[108:109], v[108:109], v[116:117] op_sel_hi:[1,0]
	v_lshl_add_u64 v[116:117], v[60:61], 0, s[66:67]
	v_pk_fma_f32 v[110:111], v[94:95], v[110:111], v[12:13]
	v_pk_fma_f32 v[112:113], v[98:99], v[112:113], v[8:9]
	global_store_dwordx2 v[116:117], v[114:115], off
	v_mov_b32_e32 v114, v193
	v_mov_b32_e32 v115, v193
	v_cvt_pk_fp8_f32 v114, v110, v111
	v_cvt_pk_fp8_f32 v115, v112, v113
	v_pk_fma_f32 v[106:107], v[92:93], v[106:107], v[14:15]
	v_pk_fma_f32 v[108:109], v[96:97], v[108:109], v[10:11]
	v_cvt_pk_fp8_f32 v114, v106, v107 op_sel:[0,0,1]
	v_cvt_pk_fp8_f32 v115, v108, v109 op_sel:[0,0,1]
	v_lshl_add_u64 v[116:117], v[58:59], 0, s[66:67]
	v_add_co_u32_e32 v116, vcc, s18, v116
	s_nop 1
	v_addc_co_u32_e32 v117, vcc, 0, v117, vcc
	global_store_dwordx2 v[116:117], v[114:115], off offset:512
	v_bfe_u32 v114, v100, 16, 1
	v_add3_u32 v100, v100, v114, s15
	v_bfe_u32 v114, v101, 16, 1
	v_lshrrev_b32_e32 v100, 16, v100
	v_add3_u32 v101, v101, v114, s15
	v_and_or_b32 v100, v101, s16, v100
	v_bfe_u32 v101, v118, 16, 1
	v_add3_u32 v101, v118, v101, s15
	v_bfe_u32 v114, v119, 16, 1
	v_lshrrev_b32_e32 v101, 16, v101
	v_add3_u32 v114, v119, v114, s15
	v_and_or_b32 v101, v114, s16, v101
	v_bfe_u32 v114, v102, 16, 1
	v_add3_u32 v102, v102, v114, s15
	v_bfe_u32 v114, v103, 16, 1
	v_lshrrev_b32_e32 v102, 16, v102
	v_add3_u32 v103, v103, v114, s15
	v_and_or_b32 v102, v103, s16, v102
	v_bfe_u32 v103, v104, 16, 1
	v_add3_u32 v103, v104, v103, s15
	v_bfe_u32 v104, v105, 16, 1
	v_lshrrev_b32_e32 v103, 16, v103
	v_add3_u32 v104, v105, v104, s15
	v_and_or_b32 v103, v104, s16, v103
	ds_write_b128 v143, v[100:103] offset:2064
	v_bfe_u32 v100, v110, 16, 1
	v_add3_u32 v100, v110, v100, s15
	v_bfe_u32 v101, v111, 16, 1
	v_lshrrev_b32_e32 v100, 16, v100
	v_add3_u32 v101, v111, v101, s15
	v_and_or_b32 v100, v101, s16, v100
	v_bfe_u32 v101, v106, 16, 1
	v_add3_u32 v101, v106, v101, s15
	v_bfe_u32 v102, v107, 16, 1
	v_lshrrev_b32_e32 v101, 16, v101
	v_add3_u32 v102, v107, v102, s15
	v_and_or_b32 v101, v102, s16, v101
	v_bfe_u32 v102, v112, 16, 1
	v_add3_u32 v102, v112, v102, s15
	v_bfe_u32 v103, v113, 16, 1
	v_lshrrev_b32_e32 v102, 16, v102
	v_add3_u32 v103, v113, v103, s15
	v_and_or_b32 v102, v103, s16, v102
	v_bfe_u32 v103, v108, 16, 1
	v_add3_u32 v103, v108, v103, s15
	v_bfe_u32 v104, v109, 16, 1
	v_lshrrev_b32_e32 v103, 16, v103
	v_add3_u32 v104, v109, v104, s15
	v_and_or_b32 v103, v104, s16, v103
	ds_write_b128 v143, v[100:103] offset:3088
	s_cbranch_scc0 .LBB0_960
; #define LAS __attribute__((address_space(3)))
; DI void phase_tail(const Frame& F, int l) {
;     ...
;         __syncthreads();
;         { f32x16 acc;
; #pragma unroll
;           for (int i = 0; i < 16; ++i) acc[i] = 0.f;
; #pragma unroll
;           for (int s = 0; s < 8; ++s) { const bf16x8 af = *(const LAS bf16x8*)(Ht + r * HT_STRIDE + 128 * F.wave + 16 * s + 8 * h);
;               acc = __builtin_amdgcn_mfma_f32_32x32x16_bf16(af, RWf[s], acc, 0, 0, 0); }
; #pragma unroll
;           for (int i = 0; i < 16; ++i) Pz[(F.wave * 32 + ((i & 3) + 8 * (i >> 2) + 4 * h)) * 32 + r] = acc[i]; }
;         __syncthreads();
	s_waitcnt lgkmcnt(0)
	s_barrier
	ds_read_b128 v[0:3], v141
	ds_read_b128 v[62:65], v141 offset:32
	s_lshl_b32 s10, s24, 5
	s_mov_b32 s2, 0
	s_mov_b64 s[66:67], -1
	v_add_u32_e32 v68, 0x400, v142
	s_waitcnt lgkmcnt(1)
	v_mfma_f32_32x32x16_bf16 v[0:15], v[0:3], v[16:19], 0
	v_add_u32_e32 v69, 0x800, v142
	v_add_u32_e32 v70, 0xc00, v142
	s_waitcnt lgkmcnt(0)
	v_mfma_f32_32x32x16_bf16 v[0:15], v[62:65], v[20:23], v[0:15]
	ds_read_b128 v[62:65], v141 offset:64
	s_waitcnt lgkmcnt(0)
	v_mfma_f32_32x32x16_bf16 v[0:15], v[62:65], v[24:27], v[0:15]
	ds_read_b128 v[62:65], v141 offset:96
	s_waitcnt lgkmcnt(0)
	v_mfma_f32_32x32x16_bf16 v[0:15], v[62:65], v[28:31], v[0:15]
	ds_read_b128 v[62:65], v141 offset:128
	s_waitcnt lgkmcnt(0)
	v_mfma_f32_32x32x16_bf16 v[0:15], v[62:65], v[32:35], v[0:15]
	ds_read_b128 v[62:65], v141 offset:160
	s_waitcnt lgkmcnt(0)
	v_mfma_f32_32x32x16_bf16 v[0:15], v[62:65], v[36:39], v[0:15]
	ds_read_b128 v[62:65], v141 offset:192
	s_waitcnt lgkmcnt(0)
	v_mfma_f32_32x32x16_bf16 v[0:15], v[62:65], v[40:43], v[0:15]
	ds_read_b128 v[62:65], v141 offset:224
	s_waitcnt lgkmcnt(0)
	v_mfma_f32_32x32x16_bf16 v[0:15], v[62:65], v[44:47], v[0:15]
	s_nop 11
	ds_write2_b32 v142, v0, v1 offset1:32
	ds_write2_b32 v142, v2, v3 offset0:64 offset1:96
	ds_write2_b32 v68, v4, v5 offset1:32
	ds_write2_b32 v68, v6, v7 offset0:64 offset1:96
	ds_write2_b32 v69, v8, v9 offset1:32
	ds_write2_b32 v69, v10, v11 offset0:64 offset1:96
	ds_write2_b32 v70, v12, v13 offset1:32
	ds_write2_b32 v70, v14, v15 offset0:64 offset1:96
	s_waitcnt lgkmcnt(0)
	s_barrier
	s_branch .LBB0_963
